# v13 plus: recurrence consumers issue the next block's output-gate loads at the top of the period (spare VGPRs) instead of just before the epilogue
# baseline (speedup 1.0000x reference)
.LBB0_355:
	s_waitcnt vmcnt(0)
	v_mov_b64_e32 v[52:53], v[234:235]
	v_mov_b64_e32 v[38:39], v[232:233]
	v_add_u32_e32 v104, 0x100, v104
	v_lshl_add_u64 v[102:103], v[102:103], 0, s[24:25]
	s_cmp_lg_u32 s36, 32
	s_mov_b32 s84, s36
	v_mov_b64_e32 v[54:55], v[236:237]
	v_mov_b64_e32 v[36:37], v[230:231]
	s_cbranch_scc0 .LBB0_380
.LBB0_356:
	s_add_i32 s36, s84, 1
	s_cmp_lg_u32 s84, 31
	s_cselect_b64 s[4:5], -1, 0
	s_cmp_eq_u32 s84, 31
	s_cbranch_scc1 .LBB0_368
	s_cmp_eq_u32 s36, 0
	s_cbranch_scc1 .Lgate_skip_g
	global_load_dwordx4 v[230:233], v[102:103], off
	global_load_dwordx4 v[234:237], v[102:103], off offset:-16
.Lgate_skip_g:
	s_andn2_b64 vcc, exec, s[26:27]
	s_cbranch_vccnz .LBB0_367
	v_ashrrev_i32_e32 v18, 5, v104
	v_mad_i64_i32 v[30:31], s[16:17], v18, s62, v[114:115]
	v_and_b32_e32 v32, 0x7ff, v18
	global_load_dwordx4 v[18:21], v[30:31], off offset:512
	global_load_dwordx4 v[22:25], v[30:31], off offset:1024
	v_cmp_ne_u32_e32 vcc, 0, v32
	s_and_saveexec_b64 s[16:17], vcc
	s_xor_b64 s[16:17], exec, s[16:17]
	s_cbranch_execz .LBB0_360
	v_add_co_u32_e32 v40, vcc, 0xfffff000, v30
	s_nop 1
	v_addc_co_u32_e32 v41, vcc, -1, v31, vcc
	global_load_dwordx4 v[26:29], v[40:41], off offset:-2048
	s_nop 0
	global_load_dwordx4 v[40:43], v[40:41], off offset:-1536

.LBB0_372:
	s_andn2_b64 vcc, exec, s[16:17]
	s_cbranch_vccz .LBB0_374
	v_mov_b64_e32 v[230:231], v[36:37]
	v_mov_b64_e32 v[236:237], v[54:55]
	v_mov_b64_e32 v[232:233], v[38:39]
	v_mov_b64_e32 v[234:235], v[52:53]

.LBB0_406:
	s_waitcnt vmcnt(0)
	v_mov_b64_e32 v[64:65], v[234:235]
	v_mov_b64_e32 v[26:27], v[230:231]
	v_add_u32_e32 v147, 0x100, v147
	v_lshl_add_u64 v[150:151], v[150:151], 0, s[24:25]
	s_cmp_lg_u32 s53, 32
	s_mov_b32 s84, s53
	v_mov_b64_e32 v[66:67], v[236:237]
	v_mov_b64_e32 v[28:29], v[232:233]
	s_cbranch_scc0 .LBB0_430
.LBB0_407:
	s_add_i32 s53, s84, 1
	s_cmp_lg_u32 s84, 31
	v_cndmask_b32_e64 v30, 0, 1, s[26:27]
	s_cselect_b64 s[16:17], -1, 0
	s_cmp_eq_u32 s84, 31
	v_cmp_ne_u32_e64 s[4:5], 1, v30
	s_cbranch_scc1 .LBB0_419
	s_cmp_eq_u32 s53, 0
	s_cbranch_scc1 .Lgate_skip_h
	global_load_dwordx4 v[230:233], v[150:151], off offset:16
	global_load_dwordx4 v[234:237], v[150:151], off
.Lgate_skip_h:
	s_and_b64 vcc, exec, s[4:5]
	s_cbranch_vccnz .LBB0_418
	v_ashrrev_i32_e32 v18, 5, v147
	v_mad_i64_i32 v[30:31], s[22:23], v18, s62, v[114:115]
	v_and_b32_e32 v32, 0x7ff, v18
	global_load_dwordx4 v[18:21], v[30:31], off offset:512
	global_load_dwordx4 v[22:25], v[30:31], off offset:1024
	v_cmp_ne_u32_e32 vcc, 0, v32
	s_and_saveexec_b64 s[22:23], vcc
	s_xor_b64 s[22:23], exec, s[22:23]
	s_cbranch_execz .LBB0_411
	v_add_co_u32_e32 v40, vcc, 0xfffff000, v30
	s_nop 1
	v_addc_co_u32_e32 v41, vcc, -1, v31, vcc
	global_load_dwordx4 v[36:39], v[40:41], off offset:-2048
	s_nop 0
	global_load_dwordx4 v[40:43], v[40:41], off offset:-1536

.LBB0_423:
	s_andn2_b64 vcc, exec, s[22:23]
	s_cbranch_vccz .LBB0_425
	v_mov_b64_e32 v[232:233], v[28:29]
	v_mov_b64_e32 v[236:237], v[66:67]
	v_mov_b64_e32 v[230:231], v[26:27]
	v_mov_b64_e32 v[234:235], v[64:65]
